# speedup vs baseline: 1.0050x; 1.0050x over previous
.LBB1_189:
	v_add_u32_e32 v165, 0x200, v165
	v_cmp_lt_u32_e32 vcc, s4, v165
	ds_write_b16 v163, v0
	s_or_b64 s[2:3], vcc, s[2:3]
	v_add_u32_e32 v163, 0x400, v163
	s_andn2_b64 exec, exec, s[2:3]
	s_cbranch_execnz .LBB1_189
	s_or_b64 exec, exec, s[2:3]
	s_and_b64 s[2:3], s[0:1], exec
	s_cselect_b32 s2, 0, 0x7ff000
	s_add_u32 s2, s28, s2
	s_addc_u32 s3, s29, 0
	v_lshlrev_b32_e32 v186, 2, v170
	s_waitcnt lgkmcnt(0)
	s_barrier
	v_lshlrev_b32_e32 v184, 2, v164
	global_load_dwordx4 v[138:141], v186, s[2:3]
	global_load_dwordx4 v[142:145], v184, s[2:3]
	v_mov_b32_e32 v165, 0
	s_bitcmp1_b32 s12, 0
	s_mov_b32 s15, 0
	v_cmp_eq_u32_e64 s[2:3], 0, v171
	v_lshl_add_u32 v187, v173, 1, v195
	s_mov_b32 s19, 64
	s_mov_b32 s16, 0x48800000
	s_mov_b32 s18, 0x36800000
	s_mov_b32 s24, 0x44800000
	v_mov_b32_e32 v188, 1
	v_lshlrev_b32_e32 v0, 3, v174
	v_lshlrev_b32_e32 v146, 3, v176
	v_lshlrev_b32_e32 v148, 3, v178
	v_lshlrev_b32_e32 v150, 3, v180
	v_lshlrev_b32_e32 v152, 3, v182
	s_mov_b32 s13, 0
	v_lshl_add_u64 v[154:155], s[30:31], 0, v[164:165]
	v_mov_b32_e32 v167, v165
	v_mov_b32_e32 v169, v165
	v_lshlrev_b32_e32 v164, 3, v172
	v_mov_b32_e32 v156, v165
	v_mov_b32_e32 v157, v165
	s_cselect_b64 s[4:5], -1, 0
	s_waitcnt vmcnt(1)
	v_mov_b64_e32 v[130:131], v[138:139]
	s_waitcnt vmcnt(0)
	v_mov_b64_e32 v[134:135], v[142:143]
	v_mov_b64_e32 v[132:133], v[140:141]
	v_mov_b64_e32 v[136:137], v[144:145]
	s_branch .LBB1_194
